# scan helper waves: the 99 packed-f32 VALU ops (v_pk_mul/add/fma_f32) of the chunk loop split into scalar pairs (bit-identical)
# speedup vs baseline: 1.0148x; 1.0095x over previous
; #define LAS __attribute__((address_space(3)))
; #define SUM16(X) sum16_ns(X)
; __device__ __forceinline__ void scan_unit(Frame& F, const Args& a, int layer, int unit) {
;     ...
;                 const LAS float* buf = bufs + (it & 1) * SC_BUF; const LAS float* yb = sY + (it & 1) * SC_VEC;
;                 const size_t row = (size_t)b * SEQ + (size_t)(it - 2) * SC + tl; const int o = tl * 64 + c8 * 8;
;                 f32x4 y_[2], v_[2], g_[2];
; #pragma unroll
;                 for (int i = 0; i < 2; ++i) { y_[i] = *(const LAS f32x4*)(yb + o + 4 * i); v_[i] = *(const LAS f32x4*)(buf + SC_VP + o + 4 * i); }
;                 const float bon = buf[SC_BON + tl * 8 + c8];
;                 unpk8(cur.gt, g_[0], g_[1]);
;                 const float s1 = ((y_[0].x + y_[0].y) + (y_[0].z + y_[0].w)) + ((y_[1].x + y_[1].y) + (y_[1].z + y_[1].w));
;                 const float mu = sum8(s1) * (1.f / 64.f);
;                 float s2 = 0.f;
; #pragma unroll
;                 for (int i = 0; i < 2; ++i) { y_[i] = y_[i] - mu; const f32x4 q = y_[i] * y_[i]; s2 += (q.x + q.y) + (q.z + q.w); }
;                 const float rstd = __builtin_amdgcn_rsqf(sum8(s2) * (1.f / 64.f) + 64e-5f);
;                 f32x4 o_[2];
; #pragma unroll
;                 for (int i = 0; i < 2; ++i) o_[i] = (y_[i] * rstd * *(const f32x4*)(a.in[14] + po + 4 * i) + *(const f32x4*)(a.in[15] + po + 4 * i) + bon * v_[i]) * g_[i];
;                 *(v4u*)(YA + row * 1024 + ch) = pk8(o_[0], o_[1]);
;             }
;             if (it < NCH) {
;                 LAS float* buf = bufs + (it & 1) * SC_BUF;
;                 const f32x4 pkk_ = *(const f32x4*)(a.in[11] + pop), pka_ = *(const f32x4*)(a.in[12] + pop), prk_ = *(const f32x4*)(a.in[13] + pop);
;                 const f32x4 zk0 = UNP4(cur.k0), zk1 = UNP4(cur.k1), zk2 = UNP4(cur.k2), zk3 = UNP4(cur.k3);
;                 f32x4 kn0 = zk0 * pkk_, kn1 = zk1 * pkk_, kn2 = zk2 * pkk_, kn3 = zk3 * pkk_;
;                 kn0 = kn0 * __builtin_amdgcn_rsqf(fmaxf(SUM16(DOT4(kn0, kn0)), 1e-24f)); kn1 = kn1 * __builtin_amdgcn_rsqf(fmaxf(SUM16(DOT4(kn1, kn1)), 1e-24f));
;                 kn2 = kn2 * __builtin_amdgcn_rsqf(fmaxf(SUM16(DOT4(kn2, kn2)), 1e-24f)); kn3 = kn3 * __builtin_amdgcn_rsqf(fmaxf(SUM16(DOT4(kn3, kn3)), 1e-24f));
;                 const f32x4 r0 = UNP4(cur.r0), r1 = UNP4(cur.r1), v0 = UNP4(cur.v0), v1 = UNP4(cur.v1), v2 = UNP4(cur.v2);
.LBB0_1332:
	s_and_b32 s1, s20, 1
	s_mul_i32 s2, s1, 0xb900
	s_add_i32 s2, s2, 0
	v_lshl_add_u32 v10, s1, 13, v129
	v_lshl_add_u32 v6, v128, 2, s2
	ds_read_b128 v[14:17], v6 offset:38144
	ds_read_b128 v[6:9], v6 offset:38160
	ds_read_b128 v[22:25], v10
	ds_read_b128 v[10:13], v10 offset:16
	v_lshlrev_b32_e32 v26, 2, v126
	v_add3_u32 v26, s2, v141, v26
	v_lshlrev_b32_e32 v114, 16, v18
	v_and_b32_e32 v115, 0xffff0000, v18
	v_lshlrev_b32_e32 v116, 16, v19
	v_and_b32_e32 v117, 0xffff0000, v19
	v_lshlrev_b32_e32 v110, 16, v20
	v_and_b32_e32 v111, 0xffff0000, v20
	v_lshlrev_b32_e32 v112, 16, v21
	v_and_b32_e32 v113, 0xffff0000, v21
	s_waitcnt lgkmcnt(0)
	v_mov_b32_e32 v18, v22
	v_mov_b32_e32 v19, v10
	v_mov_b32_e32 v20, v23
	v_mov_b32_e32 v21, v11
	ds_read_b32 v108, v26 offset:46336
	v_add_f32_e64 v18, v18, v20
	v_add_f32_e64 v19, v19, v21
	v_mov_b32_e32 v20, v24
	v_mov_b32_e32 v21, v12
	v_mov_b32_e32 v26, v25
	v_mov_b32_e32 v27, v13
	v_add_f32_e64 v20, v20, v26
	v_add_f32_e64 v21, v21, v27
	s_mov_b32 s1, s31
	v_add_f32_e64 v18, v18, v20
	v_add_f32_e64 v19, v19, v21
	s_lshl_b64 s[2:3], s[0:1], 16
	v_add_f32_e32 v18, v18, v19
	s_nop 1
	v_add_f32_dpp v18, v18, v18 quad_perm:[1,0,3,2] row_mask:0xf bank_mask:0xf bound_ctrl:1
	s_nop 1
	v_add_f32_dpp v18, v18, v18 quad_perm:[2,3,0,1] row_mask:0xf bank_mask:0xf bound_ctrl:1
	s_nop 1
	v_add_f32_dpp v26, v18, v18 row_half_mirror row_mask:0xf bank_mask:0xf bound_ctrl:1
	v_fmamk_f32 v19, v26, 0xbc800000, v23
	v_fmamk_f32 v18, v26, 0xbc800000, v22
	v_fmamk_f32 v119, v26, 0xbc800000, v11
	v_fmamk_f32 v118, v26, 0xbc800000, v10
	v_fmamk_f32 v25, v26, 0xbc800000, v25
	v_fmac_f32_e32 v24, 0xbc800000, v26
	v_mul_f32_e64 v22, v18, v18
	v_mul_f32_e64 v23, v19, v19
	v_fmamk_f32 v13, v26, 0xbc800000, v13
	v_fmac_f32_e32 v12, 0xbc800000, v26
	v_mul_f32_e64 v26, v118, v118
	v_mul_f32_e64 v27, v119, v119
	v_mul_f32_e64 v20, v24, v24
	v_mul_f32_e64 v21, v25, v25
	v_mul_f32_e64 v10, v12, v12
	v_mul_f32_e64 v11, v13, v13
	v_mov_b32_e32 v28, v22
	v_mov_b32_e32 v29, v26
	v_mov_b32_e32 v26, v23
	v_add_f32_e64 v22, v28, v26
	v_add_f32_e64 v23, v29, v27
	v_mov_b32_e32 v26, v20
	v_mov_b32_e32 v27, v10
	v_mov_b32_e32 v10, v21
	v_add_f32_e64 v10, v26, v10
	v_add_f32_e64 v11, v27, v11
	s_nop 0
	v_add_f32_e64 v10, v22, v10
	v_add_f32_e64 v11, v23, v11
	s_nop 0
	v_add_f32_e32 v10, v10, v11
	s_nop 1
	v_add_f32_dpp v10, v10, v10 quad_perm:[1,0,3,2] row_mask:0xf bank_mask:0xf bound_ctrl:1
	s_nop 1
	v_add_f32_dpp v10, v10, v10 quad_perm:[2,3,0,1] row_mask:0xf bank_mask:0xf bound_ctrl:1
	s_nop 1
	v_add_f32_dpp v10, v10, v10 row_half_mirror row_mask:0xf bank_mask:0xf bound_ctrl:1
	v_fmamk_f32 v10, v10, 0x3c800000, v243
	v_rsq_f32_e32 v120, v10
	s_nop 0
	v_mul_f32_e64 v10, v18, v120
	v_mul_f32_e64 v11, v19, v120
	v_mul_f32_e64 v122, v24, v120
	v_mul_f32_e64 v123, v25, v120
	v_mul_f32_e64 v12, v12, v120
	v_mul_f32_e64 v13, v13, v120
	v_fma_f32 v28, v178, v122, v186
	v_fma_f32 v29, v179, v123, v187
	v_fma_f32 v10, v176, v10, v184
	v_fma_f32 v11, v177, v11, v185
	v_fma_f32 v12, v182, v12, v190
	v_fma_f32 v13, v183, v13, v191
	s_waitcnt lgkmcnt(0)
	v_fma_f32 v14, v14, v108, v10
	v_fma_f32 v15, v15, v108, v11
	v_fma_f32 v10, v16, v108, v28
	v_fma_f32 v11, v17, v108, v29
	v_mul_f32_e64 v16, v118, v120
	v_mul_f32_e64 v17, v119, v120
	v_mul_f32_e64 v14, v14, v114
	v_mul_f32_e64 v15, v15, v115
	v_fma_f32 v16, v180, v16, v188
	v_fma_f32 v17, v181, v17, v189
	v_mul_f32_e64 v10, v10, v116
	v_mul_f32_e64 v11, v11, v117
	v_fma_f32 v16, v6, v108, v16
	v_fma_f32 v17, v7, v108, v17
	v_fma_f32 v6, v8, v108, v12
	v_fma_f32 v7, v9, v108, v13
	v_mul_f32_e64 v8, v16, v110
	v_mul_f32_e64 v9, v17, v111
	v_mul_f32_e64 v6, v6, v112
	v_mul_f32_e64 v7, v7, v113
	v_cvt_pk_bf16_f32 v12, v14, v15
	v_cvt_pk_bf16_f32 v13, v10, v11
	v_cvt_pk_bf16_f32 v14, v8, v9
	s_nop 0
	v_cvt_pk_bf16_f32 v15, v6, v7
	v_lshl_add_u64 v[6:7], v[30:31], 0, s[2:3]
	global_store_dwordx4 v[6:7], v[12:15], off
	s_cmpk_gt_u32 s20, 0x7f
	s_cbranch_scc1 .LBB0_1321
.LBB0_1333:
	s_nop 1
	v_mov_b64_e32 v[14:15], v[192:193]
	v_mov_b64_e32 v[16:17], v[194:195]
	v_mov_b64_e32 v[10:11], v[196:197]
	v_mov_b64_e32 v[12:13], v[198:199]
	v_mov_b64_e32 v[6:7], v[200:201]
	v_mov_b64_e32 v[8:9], v[202:203]
	v_lshlrev_b32_e32 v118, 16, v100
	v_and_b32_e32 v119, 0xffff0000, v100
	v_lshlrev_b32_e32 v120, 16, v101
	v_and_b32_e32 v121, 0xffff0000, v101
	v_lshlrev_b32_e32 v108, 16, v102
	v_and_b32_e32 v109, 0xffff0000, v102
	v_lshlrev_b32_e32 v116, 16, v103
	v_and_b32_e32 v117, 0xffff0000, v103
	v_lshlrev_b32_e32 v112, 16, v104
	v_and_b32_e32 v113, 0xffff0000, v104
	v_lshlrev_b32_e32 v114, 16, v105
	v_and_b32_e32 v115, 0xffff0000, v105
	v_lshlrev_b32_e32 v18, 16, v106
	v_and_b32_e32 v19, 0xffff0000, v106
	v_lshlrev_b32_e32 v20, 16, v107
	v_and_b32_e32 v21, 0xffff0000, v107
	v_and_b32_e32 v156, 0xffff0000, v98
	v_lshlrev_b32_e32 v158, 16, v99
	v_and_b32_e32 v160, 0xffff0000, v99
	v_lshlrev_b32_e32 v99, 16, v87
	v_and_b32_e32 v87, 0xffff0000, v87
	v_and_b32_e32 v149, 0xffff0000, v81
	s_bitcmp1_b32 s20, 0
	v_and_b32_e32 v151, 0xffff0000, v92
	v_lshlrev_b32_e32 v152, 16, v93
	v_and_b32_e32 v153, 0xffff0000, v93
	v_lshlrev_b32_e32 v150, 16, v92
	v_lshlrev_b32_e32 v92, 16, v90
	v_and_b32_e32 v93, 0xffff0000, v90
	v_lshlrev_b32_e32 v90, 16, v91
	v_and_b32_e32 v91, 0xffff0000, v91
	v_lshlrev_b32_e32 v154, 16, v96
	v_and_b32_e32 v155, 0xffff0000, v96
	v_lshlrev_b32_e32 v96, 16, v97
	v_and_b32_e32 v97, 0xffff0000, v97
	s_cselect_b32 s1, 0xb900, 0
	s_add_i32 s1, s1, 0
	v_mov_b32_e32 v157, v0
	v_mov_b32_e32 v159, v0
	v_mov_b32_e32 v161, v0
	v_mul_f32_e64 v22, v14, v118
	v_mul_f32_e64 v23, v15, v119
	v_mul_f32_e64 v24, v16, v120
; #define UNP4(W) ((f32x4){bflo((W).x), bfhi((W).x), bflo((W).y), bfhi((W).y)})
; #define EXP4(E) ((f32x4){__builtin_amdgcn_exp2f(-1.44269504f * (E).x), __builtin_amdgcn_exp2f(-1.44269504f * (E).y), __builtin_amdgcn_exp2f(-1.44269504f * (E).z), __builtin_amdgcn_exp2f(-1.44269504f * (E).w)})
; #define SUM16(X) sum16_ns(X)
; __device__ __forceinline__ void scan_unit(Frame& F, const Args& a, int layer, int unit) {
;     ...
;                 const f32x4 zk0 = UNP4(cur.k0), zk1 = UNP4(cur.k1), zk2 = UNP4(cur.k2), zk3 = UNP4(cur.k3);
;                 f32x4 kn0 = zk0 * pkk_, kn1 = zk1 * pkk_, kn2 = zk2 * pkk_, kn3 = zk3 * pkk_;
;                 kn0 = kn0 * __builtin_amdgcn_rsqf(fmaxf(SUM16(DOT4(kn0, kn0)), 1e-24f)); kn1 = kn1 * __builtin_amdgcn_rsqf(fmaxf(SUM16(DOT4(kn1, kn1)), 1e-24f));
;                 kn2 = kn2 * __builtin_amdgcn_rsqf(fmaxf(SUM16(DOT4(kn2, kn2)), 1e-24f)); kn3 = kn3 * __builtin_amdgcn_rsqf(fmaxf(SUM16(DOT4(kn3, kn3)), 1e-24f));
;                 const f32x4 r0 = UNP4(cur.r0), r1 = UNP4(cur.r1), v0 = UNP4(cur.v0), v1 = UNP4(cur.v1), v2 = UNP4(cur.v2);
;                 const f32x4 ar0 = UNP4(cur.a0), ar1 = UNP4(cur.a1), ar2 = UNP4(cur.a2);
;                 const f32x4 e0 = UNP4(cur.e0), e1 = UNP4(cur.e1), e2 = UNP4(cur.e2);
;                 const f32x4 w0 = EXP4(e0), w1 = EXP4(e1), w2 = EXP4(e2);
;                 const f32x4 a1v = -kn1, a2v = -kn2, a3v = -kn3;
;                 const f32x4 b0 = kn0 * ar0, b1 = kn1 * ar1, b2 = kn2 * ar2;
;                 const f32x4 kp0 = zk0 * (1.f + (ar0 - 1.f) * pka_), kp1 = zk1 * (1.f + (ar1 - 1.f) * pka_), kp2 = zk2 * (1.f + (ar2 - 1.f) * pka_);
;                 const f32x4 W2 = w0 * w1, Bt = b0 * w1, Kt = kp0 * w1, x0v = a2v, x1v = w2 * a3v;
	v_mul_f32_e64 v25, v17, v121
	v_mul_f32_e64 v26, v14, v108
	v_mul_f32_e64 v27, v15, v109
	v_mul_f32_e64 v28, v16, v116
	v_mul_f32_e64 v29, v17, v117
	v_mul_f32_e64 v100, v14, v112
	v_mul_f32_e64 v101, v15, v113
	v_mul_f32_e64 v102, v16, v114
	v_mul_f32_e64 v103, v17, v115
	v_mul_f32_e64 v20, v16, v20
	v_mul_f32_e64 v21, v17, v21
	v_mul_f32_e64 v18, v14, v18
	v_mul_f32_e64 v19, v15, v19
	v_mul_f32_e64 v14, v24, v24
	v_mul_f32_e64 v15, v25, v25
	v_mul_f32_e64 v16, v22, v22
	v_mul_f32_e64 v17, v23, v23
	v_mul_f32_e64 v104, v28, v28
	v_mul_f32_e64 v105, v29, v29
	v_mul_f32_e64 v106, v26, v26
	v_mul_f32_e64 v107, v27, v27
	v_pk_mov_b32 v[146:147], v[16:17], v[14:15] op_sel:[1,0]
	v_mov_b32_e32 v17, v15
	v_pk_mov_b32 v[14:15], v[106:107], v[104:105] op_sel:[1,0]
	v_mov_b32_e32 v107, v105
	v_mul_f32_e64 v110, v102, v102
	v_mul_f32_e64 v111, v103, v103
	v_mul_f32_e64 v122, v100, v100
	v_mul_f32_e64 v123, v101, v101
	v_add_f32_e64 v16, v146, v16
	v_add_f32_e64 v17, v147, v17
	v_add_f32_e64 v14, v14, v106
	v_add_f32_e64 v15, v15, v107
	v_pk_mov_b32 v[104:105], v[122:123], v[110:111] op_sel:[1,0]
	v_mov_b32_e32 v123, v111
	v_add_f32_e32 v16, v16, v17
	v_add_f32_e32 v14, v14, v15
	v_mul_f32_e32 v145, v19, v19
	v_mul_f32_e32 v148, v21, v21
	v_add_f32_e64 v104, v104, v122
	v_add_f32_e64 v105, v105, v123
	v_add_f32_dpp v16, v16, v16 quad_perm:[1,0,3,2] row_mask:0xf bank_mask:0xf bound_ctrl:1
	v_add_f32_dpp v14, v14, v14 quad_perm:[1,0,3,2] row_mask:0xf bank_mask:0xf bound_ctrl:1
	v_fmac_f32_e32 v145, v18, v18
	v_fmac_f32_e32 v148, v20, v20
	v_add_f32_e32 v15, v104, v105
	v_add_f32_e32 v106, v145, v148
	v_lshlrev_b32_e32 v122, 16, v98
	v_add_f32_dpp v15, v15, v15 quad_perm:[1,0,3,2] row_mask:0xf bank_mask:0xf bound_ctrl:1
	v_add_f32_dpp v16, v16, v16 quad_perm:[2,3,0,1] row_mask:0xf bank_mask:0xf bound_ctrl:1
	v_add_f32_dpp v14, v14, v14 quad_perm:[2,3,0,1] row_mask:0xf bank_mask:0xf bound_ctrl:1
	v_add_f32_dpp v17, v106, v106 quad_perm:[1,0,3,2] row_mask:0xf bank_mask:0xf bound_ctrl:1
	v_lshlrev_b32_e32 v98, 16, v86
	v_and_b32_e32 v86, 0xffff0000, v86
	v_add_f32_dpp v15, v15, v15 quad_perm:[2,3,0,1] row_mask:0xf bank_mask:0xf bound_ctrl:1
	v_add_f32_dpp v16, v16, v16 row_half_mirror row_mask:0xf bank_mask:0xf bound_ctrl:1
	v_add_f32_dpp v14, v14, v14 row_half_mirror row_mask:0xf bank_mask:0xf bound_ctrl:1
	v_add_f32_dpp v17, v17, v17 quad_perm:[2,3,0,1] row_mask:0xf bank_mask:0xf bound_ctrl:1
	v_lshlrev_b32_e32 v110, 16, v95
	v_and_b32_e32 v95, 0xffff0000, v95
	v_add_f32_dpp v15, v15, v15 row_half_mirror row_mask:0xf bank_mask:0xf bound_ctrl:1
	v_add_f32_dpp v16, v16, v16 row_mirror row_mask:0xf bank_mask:0xf bound_ctrl:1
	v_add_f32_dpp v14, v14, v14 row_mirror row_mask:0xf bank_mask:0xf bound_ctrl:1
	v_add_f32_dpp v17, v17, v17 row_half_mirror row_mask:0xf bank_mask:0xf bound_ctrl:1
	v_lshlrev_b32_e32 v146, 16, v80
	v_max_f32_e32 v16, v16, v16
	v_add_f32_dpp v15, v15, v15 row_mirror row_mask:0xf bank_mask:0xf bound_ctrl:1
	v_max_f32_e32 v14, v14, v14
	v_add_f32_dpp v107, v17, v17 row_mirror row_mask:0xf bank_mask:0xf bound_ctrl:1
	v_max_f32_e32 v16, 0x179abe15, v16
	v_max_f32_e32 v17, 0x179abe15, v14
	v_max_f32_e32 v15, v15, v15
	v_rsq_f32_e32 v14, v16
	v_rsq_f32_e32 v16, v17
	v_max_f32_e32 v15, 0x179abe15, v15
	v_rsq_f32_e32 v106, v15
	v_mul_f32_e64 v104, v26, v16
	v_mul_f32_e64 v105, v27, v16
	v_mul_f32_e64 v26, v28, v16
	v_mul_f32_e64 v27, v29, v16
	v_max_f32_e32 v28, v107, v107
	v_max_f32_e32 v28, 0x179abe15, v28
	v_mul_f32_e64 v24, v24, v14
	v_mul_f32_e64 v25, v25, v14
	v_mul_f32_e64 v22, v22, v14
	v_mul_f32_e64 v23, v23, v14
	v_mul_f32_e64 v16, v100, v106
	v_mul_f32_e64 v17, v101, v106
	v_mul_f32_e64 v14, v102, v106
	v_mul_f32_e64 v15, v103, v106
	v_rsq_f32_e32 v106, v28
	v_lshlrev_b32_e32 v28, 16, v88
	v_and_b32_e32 v29, 0xffff0000, v88
	v_lshlrev_b32_e32 v88, 16, v78
	v_and_b32_e32 v78, 0xffff0000, v78
	v_lshlrev_b32_e32 v100, 16, v82
	v_and_b32_e32 v101, 0xffff0000, v82
	v_lshlrev_b32_e32 v102, 16, v83
	v_and_b32_e32 v103, 0xffff0000, v83
	v_lshlrev_b32_e32 v82, 16, v89
	v_and_b32_e32 v83, 0xffff0000, v89
	v_lshlrev_b32_e32 v89, 16, v79
	v_mul_f32_e32 v78, 0xbfb8aa3b, v78
	v_and_b32_e32 v79, 0xffff0000, v79
	v_exp_f32_e32 v163, v78
	v_mul_f32_e32 v78, 0xbfb8aa3b, v89
	v_exp_f32_e32 v164, v78
	v_mul_f32_e32 v78, 0xbfb8aa3b, v79
	v_exp_f32_e32 v165, v78
	v_mul_f32_e32 v78, 0xbfb8aa3b, v98
	v_exp_f32_e32 v166, v78
	v_mul_f32_e32 v78, 0xbfb8aa3b, v86
	v_exp_f32_e32 v167, v78
	v_mul_f32_e32 v78, 0xbfb8aa3b, v99
	v_lshlrev_b32_e32 v107, 16, v94
	v_exp_f32_e32 v168, v78
	v_mul_f32_e32 v78, 0xbfb8aa3b, v87
	v_and_b32_e32 v94, 0xffff0000, v94
	v_exp_f32_e32 v169, v78
	v_mul_f32_e32 v78, 0xbfb8aa3b, v107
	v_exp_f32_e32 v170, v78
	v_mul_f32_e32 v78, 0xbfb8aa3b, v94
	v_exp_f32_e32 v171, v78
	v_mul_f32_e32 v78, 0xbfb8aa3b, v110
	v_and_b32_e32 v147, 0xffff0000, v80
	v_lshlrev_b32_e32 v148, 16, v81
	v_lshlrev_b32_e32 v80, 16, v84
	v_and_b32_e32 v81, 0xffff0000, v84
	v_mul_f32_e32 v88, 0xbfb8aa3b, v88
	v_exp_f32_e32 v172, v78
	v_mul_f32_e32 v78, 0xbfb8aa3b, v95
	v_lshlrev_b32_e32 v84, 16, v85
	v_and_b32_e32 v85, 0xffff0000, v85
	v_exp_f32_e32 v162, v88
	v_exp_f32_e32 v173, v78
	v_add_f32_e64 v78, v80, -1.0
	v_add_f32_e64 v79, v81, -1.0
	v_mul_f32_e64 v98, v20, -v106
	v_mul_f32_e64 v99, v21, -v106
	v_mul_f32_e64 v20, v22, v80
	v_mul_f32_e64 v21, v23, v81
	v_add_f32_e64 v80, v84, -1.0
	v_add_f32_e64 v81, v85, -1.0
	v_fma_f32 v78, v78, v10, 1.0
	v_fma_f32 v79, v79, v11, 1.0
	v_mul_f32_e64 v22, v24, v84
	v_mul_f32_e64 v23, v25, v85
	v_mul_f32_e64 v24, v26, v90
	v_mul_f32_e64 v25, v27, v91
	v_mul_f32_e64 v88, v104, v92
	v_mul_f32_e64 v89, v105, v93
; #define SUM16(X) sum16_ns(X)
; __device__ __forceinline__ void scan_unit(Frame& F, const Args& a, int layer, int unit) {
;     ...
;                 const f32x4 a1v = -kn1, a2v = -kn2, a3v = -kn3;
;                 const f32x4 b0 = kn0 * ar0, b1 = kn1 * ar1, b2 = kn2 * ar2;
;                 const f32x4 kp0 = zk0 * (1.f + (ar0 - 1.f) * pka_), kp1 = zk1 * (1.f + (ar1 - 1.f) * pka_), kp2 = zk2 * (1.f + (ar2 - 1.f) * pka_);
;                 const f32x4 W2 = w0 * w1, Bt = b0 * w1, Kt = kp0 * w1, x0v = a2v, x1v = w2 * a3v;
;                 const f32x4 X0 = W2 * x0v, X1 = W2 * x1v, X2 = w0 * r0, X3 = W2 * r1;
;                 *(LAS f32x4*)(buf + SC_WW + pr * 64 + c4 * 4) = W2;
;                 *(LAS f32x4*)(buf + SC_VP + (2 * pr) * 64 + c4 * 4) = v0; *(LAS f32x4*)(buf + SC_VP + (2 * pr + 1) * 64 + c4 * 4) = v1;
;                 { LAS f32x4* vq = (LAS f32x4*)(buf + SC_VQ + pr * 256 + c4 * 16);
;                   vq[0] = (f32x4){v0.x, v1.x, v2.x, 0.f}; vq[1] = (f32x4){v0.y, v1.y, v2.y, 0.f}; vq[2] = (f32x4){v0.z, v1.z, v2.z, 0.f}; vq[3] = (f32x4){v0.w, v1.w, v2.w, 0.f}; }
;                 { LAS v2u* bkp = (LAS v2u*)(buf + SC_BK + pr * 128) + (((c4 & 3) * 4) * 4 + (c4 >> 2));
;                   bkp[0] = (v2u){cvt_pk_bf16(Bt.x, Kt.x), cvt_pk_bf16(b1.x, kp1.x)}; bkp[4] = (v2u){cvt_pk_bf16(Bt.y, Kt.y), cvt_pk_bf16(b1.y, kp1.y)};
;                   bkp[8] = (v2u){cvt_pk_bf16(Bt.z, Kt.z), cvt_pk_bf16(b1.z, kp1.z)}; bkp[12] = (v2u){cvt_pk_bf16(Bt.w, Kt.w), cvt_pk_bf16(b1.w, kp1.w)}; }
;                 { LAS unsigned char* xp = (LAS unsigned char*)(buf + SC_XA) + pr * 512 + (c4 >> 3) * 64 + (c4 & 3) * 16 + ((c4 >> 2) & 1) * 8;
;                   *(LAS v2u*)xp = (v2u){cvt_pk_bf16(X0.x, X0.y), cvt_pk_bf16(X0.z, X0.w)}; *(LAS v2u*)(xp + 128) = (v2u){cvt_pk_bf16(X1.x, X1.y), cvt_pk_bf16(X1.z, X1.w)};
;                   *(LAS v2u*)(xp + 256) = (v2u){cvt_pk_bf16(X2.x, X2.y), cvt_pk_bf16(X2.z, X2.w)}; *(LAS v2u*)(xp + 384) = (v2u){cvt_pk_bf16(X3.x, X3.y), cvt_pk_bf16(X3.z, X3.w)}; }
;                 const f32x4 ca = (f32x4){SUM16(DOT4(Bt, x0v)), SUM16(DOT4(Kt, x0v)), SUM16(DOT4(b1, x0v)), SUM16(DOT4(kp1, x0v))};
;                 const f32x4 cb = (f32x4){SUM16(DOT4(Bt, x1v)), SUM16(DOT4(Kt, x1v)), SUM16(DOT4(b1, x1v)), SUM16(DOT4(kp1, x1v))};
;                 const f32x4 cc = (f32x4){SUM16(DOT4(b2, a3v)), SUM16(DOT4(kp2, a3v)), SUM16(DOT4(b0, r0)), SUM16(DOT4(kp0, r0))};
	v_fma_f32 v84, v80, v12, 1.0
	v_fma_f32 v85, v81, v13, 1.0
	v_mul_f32_e64 v80, v78, v118
	v_mul_f32_e64 v81, v79, v119
	v_add_f32_e64 v78, v90, -1.0
	v_add_f32_e64 v79, v91, -1.0
	v_add_f32_e64 v86, v92, -1.0
	v_add_f32_e64 v87, v93, -1.0
	v_add_f32_e64 v90, v96, -1.0
	v_add_f32_e64 v91, v97, -1.0
	v_add_f32_e64 v92, v154, -1.0
	v_add_f32_e64 v93, v155, -1.0
	v_mul_f32_e64 v84, v84, v120
	v_mul_f32_e64 v85, v85, v121
	v_fma_f32 v86, v86, v10, 1.0
	v_fma_f32 v87, v87, v11, 1.0
	v_fma_f32 v78, v78, v12, 1.0
	v_fma_f32 v79, v79, v13, 1.0
	v_fma_f32 v10, v92, v10, 1.0
	v_fma_f32 v11, v93, v11, 1.0
	v_fma_f32 v12, v90, v12, 1.0
	v_fma_f32 v13, v91, v13, 1.0
	v_lshlrev_b32_e32 v120, 2, v127
	v_mul_f32_e64 v107, v19, -v106
	v_mul_f32_e64 v106, v18, -v106
	v_mul_f32_e64 v78, v78, v116
	v_mul_f32_e64 v79, v79, v117
	v_mul_f32_e64 v86, v86, v108
	v_mul_f32_e64 v87, v87, v109
	v_mul_f32_e64 v108, v12, v114
	v_mul_f32_e64 v109, v13, v115
	v_mul_f32_e64 v112, v10, v112
	v_mul_f32_e64 v113, v11, v113
	v_mul_f32_e64 v12, v168, v164
	v_mul_f32_e64 v13, v169, v165
	v_mul_f32_e64 v10, v166, v162
	v_mul_f32_e64 v11, v167, v163
	v_mul_f32_e64 v116, v172, v98
	v_mul_f32_e64 v117, v173, v99
	v_add3_u32 v121, s1, v130, v120
	v_mul_f32_e64 v94, v168, v22
	v_mul_f32_e64 v95, v169, v23
	v_mul_f32_e64 v90, v168, v84
	v_mul_f32_e64 v91, v169, v85
	v_mul_f32_e64 v114, v170, v106
	v_mul_f32_e64 v115, v171, v107
	v_mul_f32_e64 v118, v12, -v14
	v_mul_f32_e64 v119, v13, -v15
	v_mul_f32_e64 v168, v12, v116
	v_mul_f32_e64 v169, v13, v117
	v_mul_f32_e64 v172, v82, v12
	v_mul_f32_e64 v173, v83, v13
	ds_write_b128 v121, v[10:13]
	v_add_u32_e32 v12, s1, v131
	v_mul_f32_e64 v18, v14, v96
	v_mul_f32_e64 v19, v15, v97
	v_mul_f32_e64 v96, v166, v20
	v_mul_f32_e64 v97, v167, v21
	v_mul_f32_e64 v92, v166, v80
	v_mul_f32_e64 v93, v167, v81
	v_mul_f32_e64 v166, v10, -v16
	v_mul_f32_e64 v167, v11, -v17
	v_mul_f32_e64 v170, v10, v114
	v_mul_f32_e64 v171, v11, v115
	v_mul_f32_e64 v174, v28, v10
	v_mul_f32_e64 v175, v29, v11
	v_add_u32_e32 v10, v12, v120
	ds_write_b128 v10, v[146:149] offset:38144
	v_add3_u32 v10, s1, v132, v120
	v_mul_f32_e64 v110, v16, v154
	v_mul_f32_e64 v111, v17, v155
	ds_write_b128 v10, v[150:153] offset:38144
	v_add3_u32 v10, s1, v133, v134
	v_mov_b32_e32 v154, v147
	v_mov_b32_e32 v155, v151
	ds_write_b128 v10, v[154:157] offset:4112
	v_mov_b32_e32 v156, v148
	v_mov_b32_e32 v157, v152
	v_mov_b32_e32 v120, v146
	v_mov_b32_e32 v121, v150
	v_mov_b32_e32 v123, v0
	ds_write_b128 v10, v[156:159] offset:4128
	v_mov_b32_e32 v158, v149
	v_mov_b32_e32 v159, v153
	ds_write_b128 v10, v[120:123] offset:4096
	ds_write_b128 v10, v[158:161] offset:4144
	v_add3_u32 v13, v12, v135, v142
	v_cvt_pk_bf16_f32 v10, v96, v92
	v_cvt_pk_bf16_f32 v11, v88, v86
	ds_write_b64 v13, v[10:11] offset:20480
	v_cvt_pk_bf16_f32 v10, v97, v93
	v_cvt_pk_bf16_f32 v11, v89, v87
	ds_write_b64 v13, v[10:11] offset:20512
	v_cvt_pk_bf16_f32 v10, v94, v90
	v_cvt_pk_bf16_f32 v11, v24, v78
	ds_write_b64 v13, v[10:11] offset:20544
	v_cvt_pk_bf16_f32 v10, v95, v91
	v_cvt_pk_bf16_f32 v11, v25, v79
	ds_write_b64 v13, v[10:11] offset:20576
	v_add_u32_e32 v10, v12, v136
	v_add3_u32 v12, v10, v137, v138
	v_cvt_pk_bf16_f32 v10, v166, v167
	v_cvt_pk_bf16_f32 v11, v118, v119
	ds_write_b64 v12, v[10:11] offset:28672
	v_cvt_pk_bf16_f32 v10, v170, v171
	v_cvt_pk_bf16_f32 v11, v168, v169
	v_mul_f32_e64 v164, v164, v102
	v_mul_f32_e64 v165, v165, v103
	v_mul_f32_e64 v162, v162, v100
	v_mul_f32_e64 v163, v163, v101
	ds_write_b64 v12, v[10:11] offset:28800
	v_cvt_pk_bf16_f32 v10, v162, v163
	v_cvt_pk_bf16_f32 v11, v164, v165
	ds_write_b64 v12, v[10:11] offset:28928
	v_cvt_pk_bf16_f32 v10, v174, v175
	v_cvt_pk_bf16_f32 v11, v172, v173
	ds_write_b64 v12, v[10:11] offset:29056
	v_mul_f32_e64 v10, v97, -v17
	v_mul_f32_e64 v11, v95, -v15
	v_fma_f32 v10, v96, -v16, v10
	v_fma_f32 v11, v94, -v14, v11
	v_add_f32_e32 v10, v10, v11
	v_mul_f32_e64 v11, v93, -v17
	v_mul_f32_e64 v12, v91, -v15
	v_fma_f32 v11, v92, -v16, v11
	v_fma_f32 v12, v90, -v14, v12
	v_add_f32_e32 v11, v11, v12
	v_mul_f32_e64 v12, v89, -v17
	v_mul_f32_e64 v13, v25, -v15
	v_fma_f32 v12, v88, -v16, v12
	v_fma_f32 v13, v24, -v14, v13
	v_add_f32_e32 v12, v12, v13
	v_mul_f32_e64 v13, v87, -v17
	v_mul_f32_e64 v15, v79, -v15
	v_fma_f32 v13, v86, -v16, v13
	v_fma_f32 v14, v78, -v14, v15
	v_add_f32_e32 v13, v13, v14
	v_mul_f32_e32 v14, v97, v115
	v_mul_f32_e32 v15, v95, v117
	v_fmac_f32_e32 v14, v96, v114
	v_fmac_f32_e32 v15, v94, v116
	v_add_f32_e32 v14, v14, v15
	v_mul_f32_e32 v15, v93, v115
	v_mul_f32_e32 v16, v91, v117
	v_mul_f32_e32 v21, v21, v101
	v_fmac_f32_e32 v15, v92, v114
	v_fmac_f32_e32 v16, v90, v116
	v_fmac_f32_e32 v21, v20, v100
	v_mul_f32_e32 v20, v23, v103
	v_add_f32_e32 v15, v15, v16
	v_mul_f32_e32 v16, v89, v115
	v_mul_f32_e32 v17, v25, v117
	v_fmac_f32_e32 v20, v22, v102
	v_mul_f32_e32 v89, v89, v29
	v_mul_f32_e32 v25, v25, v83
	v_add_f32_e32 v20, v21, v20
	v_mul_f32_e32 v21, v81, v101
	v_mul_f32_e32 v22, v85, v103
	v_fmac_f32_e32 v89, v88, v28
	v_fmac_f32_e32 v25, v24, v82
	v_fmac_f32_e32 v16, v88, v114
	v_fmac_f32_e32 v17, v24, v116
	v_fmac_f32_e32 v21, v80, v100
	v_fmac_f32_e32 v22, v84, v102
	v_add_f32_e32 v24, v89, v25
	v_mul_f32_e32 v25, v87, v29
	v_mul_f32_e32 v88, v79, v83
	v_add_f32_e32 v21, v21, v22
	v_mul_f32_e32 v22, v97, v29
	v_mul_f32_e32 v23, v95, v83
	v_fmac_f32_e32 v25, v86, v28
	v_fmac_f32_e32 v88, v78, v82
	v_add_f32_e32 v16, v16, v17
	v_mul_f32_e32 v17, v87, v115
	v_fmac_f32_e32 v22, v96, v28
	v_fmac_f32_e32 v23, v94, v82
	v_add_f32_e32 v25, v25, v88
	v_mul_f32_e64 v88, v81, -v105
	v_mul_f32_e64 v27, v85, -v27
	v_fmac_f32_e32 v17, v86, v114
; #define SUM16(X) sum16_ns(X)
; __device__ __forceinline__ void scan_unit(Frame& F, const Args& a, int layer, int unit) {
;     ...
;                 const f32x4 ca = (f32x4){SUM16(DOT4(Bt, x0v)), SUM16(DOT4(Kt, x0v)), SUM16(DOT4(b1, x0v)), SUM16(DOT4(kp1, x0v))};
;                 const f32x4 cb = (f32x4){SUM16(DOT4(Bt, x1v)), SUM16(DOT4(Kt, x1v)), SUM16(DOT4(b1, x1v)), SUM16(DOT4(kp1, x1v))};
;                 const f32x4 cc = (f32x4){SUM16(DOT4(b2, a3v)), SUM16(DOT4(kp2, a3v)), SUM16(DOT4(b0, r0)), SUM16(DOT4(kp0, r0))};
;                 const f32x4 cd = (f32x4){SUM16(DOT4(Bt, r1)), SUM16(DOT4(Kt, r1)), SUM16(DOT4(b1, r1)), SUM16(DOT4(kp1, r1))};
;                 const float ci = SUM16(DOT4(kp0, a1v));
;                 const f32x4 z0 = r0 * kp0 * prk_, z1 = r1 * kp1 * prk_;
;                 const float bon0 = SUM16((z0.x + z0.y) + (z0.z + z0.w)), bon1 = SUM16((z1.x + z1.y) + (z1.z + z1.w));
	v_mul_f32_e32 v114, v79, v117
	v_mul_f32_e32 v111, v111, v107
	v_mul_f32_e32 v19, v19, v99
	v_add_f32_e32 v22, v22, v23
	v_mul_f32_e32 v23, v93, v29
	v_fma_f32 v88, v80, -v104, v88
	v_fma_f32 v26, v84, -v26, v27
	v_mul_f32_e64 v80, v100, v80
	v_mul_f32_e64 v81, v101, v81
	v_mul_f32_e64 v84, v102, v84
	v_mul_f32_e64 v85, v103, v85
	v_fmac_f32_e32 v114, v78, v116
	v_fmac_f32_e32 v111, v110, v106
	v_fmac_f32_e32 v19, v18, v98
	v_fmac_f32_e32 v23, v92, v28
	v_mul_f32_e64 v84, v8, v84
	v_mul_f32_e64 v85, v9, v85
	v_mul_f32_e64 v80, v6, v80
	v_mul_f32_e64 v81, v7, v81
	v_mul_f32_e64 v28, v28, v86
	v_mul_f32_e64 v29, v29, v87
	v_mul_f32_e64 v78, v82, v78
	v_mul_f32_e64 v79, v83, v79
	v_add_f32_e32 v18, v111, v19
	v_mul_f32_e32 v19, v113, v107
	v_mul_f32_e32 v99, v109, v99
	v_mul_f32_e32 v91, v91, v83
	v_mul_f32_e64 v8, v8, v78
	v_mul_f32_e64 v9, v9, v79
	v_mul_f32_e64 v28, v6, v28
	v_mul_f32_e64 v29, v7, v29
	v_add_f32_e32 v6, v80, v81
	v_add_f32_e32 v7, v84, v85
	v_fmac_f32_e32 v19, v112, v106
	v_fmac_f32_e32 v99, v108, v98
	v_fmac_f32_e32 v91, v90, v82
	v_add_f32_e32 v6, v6, v7
	v_add_f32_e32 v7, v28, v29
	v_add_f32_e32 v8, v8, v9
	v_add_f32_e32 v17, v17, v114
	v_add_f32_e32 v19, v19, v99
	v_add_f32_e32 v23, v23, v91
	v_add_f32_e32 v26, v88, v26
	v_add_f32_e32 v7, v7, v8
	v_add_f32_dpp v10, v10, v10 quad_perm:[1,0,3,2] row_mask:0xf bank_mask:0xf bound_ctrl:1
	v_add_f32_dpp v11, v11, v11 quad_perm:[1,0,3,2] row_mask:0xf bank_mask:0xf bound_ctrl:1
	v_add_f32_dpp v12, v12, v12 quad_perm:[1,0,3,2] row_mask:0xf bank_mask:0xf bound_ctrl:1
	v_add_f32_dpp v13, v13, v13 quad_perm:[1,0,3,2] row_mask:0xf bank_mask:0xf bound_ctrl:1
	v_add_f32_dpp v14, v14, v14 quad_perm:[1,0,3,2] row_mask:0xf bank_mask:0xf bound_ctrl:1
	v_add_f32_dpp v15, v15, v15 quad_perm:[1,0,3,2] row_mask:0xf bank_mask:0xf bound_ctrl:1
	v_add_f32_dpp v16, v16, v16 quad_perm:[1,0,3,2] row_mask:0xf bank_mask:0xf bound_ctrl:1
	v_add_f32_dpp v17, v17, v17 quad_perm:[1,0,3,2] row_mask:0xf bank_mask:0xf bound_ctrl:1
	v_add_f32_dpp v18, v18, v18 quad_perm:[1,0,3,2] row_mask:0xf bank_mask:0xf bound_ctrl:1
	v_add_f32_dpp v19, v19, v19 quad_perm:[1,0,3,2] row_mask:0xf bank_mask:0xf bound_ctrl:1
	v_add_f32_dpp v20, v20, v20 quad_perm:[1,0,3,2] row_mask:0xf bank_mask:0xf bound_ctrl:1
	v_add_f32_dpp v21, v21, v21 quad_perm:[1,0,3,2] row_mask:0xf bank_mask:0xf bound_ctrl:1
	v_add_f32_dpp v22, v22, v22 quad_perm:[1,0,3,2] row_mask:0xf bank_mask:0xf bound_ctrl:1
	v_add_f32_dpp v23, v23, v23 quad_perm:[1,0,3,2] row_mask:0xf bank_mask:0xf bound_ctrl:1
	v_add_f32_dpp v24, v24, v24 quad_perm:[1,0,3,2] row_mask:0xf bank_mask:0xf bound_ctrl:1
	v_add_f32_dpp v25, v25, v25 quad_perm:[1,0,3,2] row_mask:0xf bank_mask:0xf bound_ctrl:1
	v_add_f32_dpp v26, v26, v26 quad_perm:[1,0,3,2] row_mask:0xf bank_mask:0xf bound_ctrl:1
	v_add_f32_dpp v6, v6, v6 quad_perm:[1,0,3,2] row_mask:0xf bank_mask:0xf bound_ctrl:1
	v_add_f32_dpp v7, v7, v7 quad_perm:[1,0,3,2] row_mask:0xf bank_mask:0xf bound_ctrl:1
	s_nop 1
	v_add_f32_dpp v10, v10, v10 quad_perm:[2,3,0,1] row_mask:0xf bank_mask:0xf bound_ctrl:1
	v_add_f32_dpp v11, v11, v11 quad_perm:[2,3,0,1] row_mask:0xf bank_mask:0xf bound_ctrl:1
	v_add_f32_dpp v12, v12, v12 quad_perm:[2,3,0,1] row_mask:0xf bank_mask:0xf bound_ctrl:1
	v_add_f32_dpp v13, v13, v13 quad_perm:[2,3,0,1] row_mask:0xf bank_mask:0xf bound_ctrl:1
	v_add_f32_dpp v14, v14, v14 quad_perm:[2,3,0,1] row_mask:0xf bank_mask:0xf bound_ctrl:1
	v_add_f32_dpp v15, v15, v15 quad_perm:[2,3,0,1] row_mask:0xf bank_mask:0xf bound_ctrl:1
	v_add_f32_dpp v16, v16, v16 quad_perm:[2,3,0,1] row_mask:0xf bank_mask:0xf bound_ctrl:1
	v_add_f32_dpp v17, v17, v17 quad_perm:[2,3,0,1] row_mask:0xf bank_mask:0xf bound_ctrl:1
	v_add_f32_dpp v18, v18, v18 quad_perm:[2,3,0,1] row_mask:0xf bank_mask:0xf bound_ctrl:1
	v_add_f32_dpp v19, v19, v19 quad_perm:[2,3,0,1] row_mask:0xf bank_mask:0xf bound_ctrl:1
	v_add_f32_dpp v20, v20, v20 quad_perm:[2,3,0,1] row_mask:0xf bank_mask:0xf bound_ctrl:1
	v_add_f32_dpp v21, v21, v21 quad_perm:[2,3,0,1] row_mask:0xf bank_mask:0xf bound_ctrl:1
	v_add_f32_dpp v22, v22, v22 quad_perm:[2,3,0,1] row_mask:0xf bank_mask:0xf bound_ctrl:1
; #define LAS __attribute__((address_space(3)))
; #define SUM16(X) sum16_ns(X)
; __device__ __forceinline__ void scan_unit(Frame& F, const Args& a, int layer, int unit) {
;     ...
;                 const f32x4 ca = (f32x4){SUM16(DOT4(Bt, x0v)), SUM16(DOT4(Kt, x0v)), SUM16(DOT4(b1, x0v)), SUM16(DOT4(kp1, x0v))};
;                 const f32x4 cb = (f32x4){SUM16(DOT4(Bt, x1v)), SUM16(DOT4(Kt, x1v)), SUM16(DOT4(b1, x1v)), SUM16(DOT4(kp1, x1v))};
;                 const f32x4 cc = (f32x4){SUM16(DOT4(b2, a3v)), SUM16(DOT4(kp2, a3v)), SUM16(DOT4(b0, r0)), SUM16(DOT4(kp0, r0))};
;                 const f32x4 cd = (f32x4){SUM16(DOT4(Bt, r1)), SUM16(DOT4(Kt, r1)), SUM16(DOT4(b1, r1)), SUM16(DOT4(kp1, r1))};
;                 const float ci = SUM16(DOT4(kp0, a1v));
;                 const f32x4 z0 = r0 * kp0 * prk_, z1 = r1 * kp1 * prk_;
;                 const float bon0 = SUM16((z0.x + z0.y) + (z0.z + z0.w)), bon1 = SUM16((z1.x + z1.y) + (z1.z + z1.w));
;                 if (c4 == 0) { LAS f32x4* cp = (LAS f32x4*)(buf + SC_C + pr * 20); cp[0] = ca; cp[1] = cb; cp[2] = cc; cp[3] = cd; cp[4] = (f32x4){ci, 0.f, 0.f, 0.f}; }
;                 buf[SC_BON + (2 * pr) * 8 + (c4 >> 1)] = bon0; buf[SC_BON + (2 * pr + 1) * 8 + (c4 >> 1)] = bon1;
	v_add_f32_dpp v23, v23, v23 quad_perm:[2,3,0,1] row_mask:0xf bank_mask:0xf bound_ctrl:1
	v_add_f32_dpp v24, v24, v24 quad_perm:[2,3,0,1] row_mask:0xf bank_mask:0xf bound_ctrl:1
	v_add_f32_dpp v25, v25, v25 quad_perm:[2,3,0,1] row_mask:0xf bank_mask:0xf bound_ctrl:1
	v_add_f32_dpp v26, v26, v26 quad_perm:[2,3,0,1] row_mask:0xf bank_mask:0xf bound_ctrl:1
	v_add_f32_dpp v6, v6, v6 quad_perm:[2,3,0,1] row_mask:0xf bank_mask:0xf bound_ctrl:1
	v_add_f32_dpp v7, v7, v7 quad_perm:[2,3,0,1] row_mask:0xf bank_mask:0xf bound_ctrl:1
	s_nop 1
	v_add_f32_dpp v10, v10, v10 row_half_mirror row_mask:0xf bank_mask:0xf bound_ctrl:1
	v_add_f32_dpp v11, v11, v11 row_half_mirror row_mask:0xf bank_mask:0xf bound_ctrl:1
	v_add_f32_dpp v12, v12, v12 row_half_mirror row_mask:0xf bank_mask:0xf bound_ctrl:1
	v_add_f32_dpp v13, v13, v13 row_half_mirror row_mask:0xf bank_mask:0xf bound_ctrl:1
	v_add_f32_dpp v14, v14, v14 row_half_mirror row_mask:0xf bank_mask:0xf bound_ctrl:1
	v_add_f32_dpp v15, v15, v15 row_half_mirror row_mask:0xf bank_mask:0xf bound_ctrl:1
	v_add_f32_dpp v16, v16, v16 row_half_mirror row_mask:0xf bank_mask:0xf bound_ctrl:1
	v_add_f32_dpp v17, v17, v17 row_half_mirror row_mask:0xf bank_mask:0xf bound_ctrl:1
	v_add_f32_dpp v18, v18, v18 row_half_mirror row_mask:0xf bank_mask:0xf bound_ctrl:1
	v_add_f32_dpp v19, v19, v19 row_half_mirror row_mask:0xf bank_mask:0xf bound_ctrl:1
	v_add_f32_dpp v20, v20, v20 row_half_mirror row_mask:0xf bank_mask:0xf bound_ctrl:1
	v_add_f32_dpp v21, v21, v21 row_half_mirror row_mask:0xf bank_mask:0xf bound_ctrl:1
	v_add_f32_dpp v22, v22, v22 row_half_mirror row_mask:0xf bank_mask:0xf bound_ctrl:1
	v_add_f32_dpp v23, v23, v23 row_half_mirror row_mask:0xf bank_mask:0xf bound_ctrl:1
	v_add_f32_dpp v24, v24, v24 row_half_mirror row_mask:0xf bank_mask:0xf bound_ctrl:1
	v_add_f32_dpp v25, v25, v25 row_half_mirror row_mask:0xf bank_mask:0xf bound_ctrl:1
	v_add_f32_dpp v26, v26, v26 row_half_mirror row_mask:0xf bank_mask:0xf bound_ctrl:1
	v_add_f32_dpp v6, v6, v6 row_half_mirror row_mask:0xf bank_mask:0xf bound_ctrl:1
	v_add_f32_dpp v7, v7, v7 row_half_mirror row_mask:0xf bank_mask:0xf bound_ctrl:1
	s_nop 1
	v_add_f32_dpp v10, v10, v10 row_mirror row_mask:0xf bank_mask:0xf bound_ctrl:1
	v_add_f32_dpp v11, v11, v11 row_mirror row_mask:0xf bank_mask:0xf bound_ctrl:1
	v_add_f32_dpp v12, v12, v12 row_mirror row_mask:0xf bank_mask:0xf bound_ctrl:1
	v_add_f32_dpp v13, v13, v13 row_mirror row_mask:0xf bank_mask:0xf bound_ctrl:1
	v_add_f32_dpp v14, v14, v14 row_mirror row_mask:0xf bank_mask:0xf bound_ctrl:1
	v_add_f32_dpp v15, v15, v15 row_mirror row_mask:0xf bank_mask:0xf bound_ctrl:1
	v_add_f32_dpp v16, v16, v16 row_mirror row_mask:0xf bank_mask:0xf bound_ctrl:1
	v_add_f32_dpp v17, v17, v17 row_mirror row_mask:0xf bank_mask:0xf bound_ctrl:1
	v_add_f32_dpp v18, v18, v18 row_mirror row_mask:0xf bank_mask:0xf bound_ctrl:1
	v_add_f32_dpp v19, v19, v19 row_mirror row_mask:0xf bank_mask:0xf bound_ctrl:1
	v_add_f32_dpp v20, v20, v20 row_mirror row_mask:0xf bank_mask:0xf bound_ctrl:1
	v_add_f32_dpp v21, v21, v21 row_mirror row_mask:0xf bank_mask:0xf bound_ctrl:1
	v_add_f32_dpp v22, v22, v22 row_mirror row_mask:0xf bank_mask:0xf bound_ctrl:1
	v_add_f32_dpp v23, v23, v23 row_mirror row_mask:0xf bank_mask:0xf bound_ctrl:1
	v_add_f32_dpp v24, v24, v24 row_mirror row_mask:0xf bank_mask:0xf bound_ctrl:1
	v_add_f32_dpp v25, v25, v25 row_mirror row_mask:0xf bank_mask:0xf bound_ctrl:1
	v_add_f32_dpp v26, v26, v26 row_mirror row_mask:0xf bank_mask:0xf bound_ctrl:1
	v_add_f32_dpp v6, v6, v6 row_mirror row_mask:0xf bank_mask:0xf bound_ctrl:1
	v_add_f32_dpp v7, v7, v7 row_mirror row_mask:0xf bank_mask:0xf bound_ctrl:1
	s_and_saveexec_b64 s[2:3], s[40:41]
	s_cbranch_execz .LBB0_1320
	v_add_u32_e32 v8, s1, v139
	v_mov_b32_e32 v27, v0
	v_mov_b32_e32 v28, v0
	v_mov_b32_e32 v29, v0
	ds_write_b128 v8, v[10:13] offset:36864
	ds_write_b128 v8, v[14:17] offset:36880
	ds_write_b128 v8, v[18:21] offset:36896
	ds_write_b128 v8, v[22:25] offset:36912
	ds_write_b128 v8, v[26:29] offset:36928
	s_branch .LBB0_1320
